# P8 v-phase ffn (X2) stores marked nt so they do not compete with the L2-resident table slice, on top of combo5
# baseline (speedup 1.0000x reference)
.LBB0_838:
	s_add_i32 s54, s54, 2
	s_waitcnt vmcnt(32)
	v_cvt_pk_f32_fp8_e32 v[156:157], v124
	v_cvt_pk_f32_fp8_sdwa v[194:195], v124 src0_sel:WORD_1
	v_cvt_pk_f32_fp8_e32 v[196:197], v125
	v_cvt_pk_f32_fp8_sdwa v[124:125], v125 src0_sel:WORD_1
	v_lshl_add_u32 v128, v139, 2, s34
	s_waitcnt vmcnt(31)
	v_cvt_pk_f32_fp8_e32 v[204:205], v120
	v_cvt_pk_f32_fp8_sdwa v[206:207], v120 src0_sel:WORD_1
	v_cvt_pk_f32_fp8_e32 v[208:209], v121
	v_cvt_pk_f32_fp8_sdwa v[120:121], v121 src0_sel:WORD_1
	ds_read_b128 v[186:189], v128 offset:2048
	ds_read_b128 v[190:193], v128 offset:2064
	ds_read_b128 v[132:135], v128 offset:2080
	ds_read_b128 v[128:131], v128 offset:2096
	v_cvt_pk_f32_fp8_e32 v[198:199], v126
	s_waitcnt lgkmcnt(3)
	v_pk_fma_f32 v[156:157], v[186:187], v[156:157], 0 op_sel_hi:[0,1,0]
	v_pk_fma_f32 v[194:195], v[186:187], v[194:195], 0 op_sel_hi:[0,1,0]
	v_pk_fma_f32 v[124:125], v[186:187], v[124:125], 0 op_sel_hi:[0,1,0]
	v_cvt_pk_f32_fp8_sdwa v[200:201], v126 src0_sel:WORD_1
	v_cvt_pk_f32_fp8_e32 v[202:203], v127
	v_cvt_pk_f32_fp8_sdwa v[126:127], v127 src0_sel:WORD_1
	v_pk_fma_f32 v[156:157], v[186:187], v[204:205], v[156:157] op_sel:[1,0,0]
	v_pk_fma_f32 v[194:195], v[186:187], v[206:207], v[194:195] op_sel:[1,0,0]
	v_pk_fma_f32 v[120:121], v[186:187], v[120:121], v[124:125] op_sel:[1,0,0]
	v_cvt_pk_f32_fp8_e32 v[124:125], v122
	v_cvt_pk_f32_fp8_sdwa v[204:205], v122 src0_sel:WORD_1
	v_cvt_pk_f32_fp8_e32 v[206:207], v123
	v_cvt_pk_f32_fp8_sdwa v[122:123], v123 src0_sel:WORD_1
	v_pk_fma_f32 v[196:197], v[186:187], v[196:197], 0 op_sel_hi:[0,1,0]
	v_pk_fma_f32 v[198:199], v[186:187], v[198:199], 0 op_sel_hi:[0,1,0]
	v_pk_fma_f32 v[200:201], v[186:187], v[200:201], 0 op_sel_hi:[0,1,0]
	v_pk_fma_f32 v[202:203], v[186:187], v[202:203], 0 op_sel_hi:[0,1,0]
	v_pk_fma_f32 v[126:127], v[186:187], v[126:127], 0 op_sel_hi:[0,1,0]
	v_pk_fma_f32 v[196:197], v[186:187], v[208:209], v[196:197] op_sel:[1,0,0]
	v_pk_fma_f32 v[124:125], v[186:187], v[124:125], v[198:199] op_sel:[1,0,0]
	v_pk_fma_f32 v[198:199], v[186:187], v[204:205], v[200:201] op_sel:[1,0,0]
	v_pk_fma_f32 v[200:201], v[186:187], v[206:207], v[202:203] op_sel:[1,0,0]
	v_pk_fma_f32 v[122:123], v[186:187], v[122:123], v[126:127] op_sel:[1,0,0]
	s_waitcnt vmcnt(30)
	v_cvt_pk_f32_fp8_e32 v[126:127], v116
	v_cvt_pk_f32_fp8_sdwa v[186:187], v116 src0_sel:WORD_1
	v_cvt_pk_f32_fp8_e32 v[202:203], v117
	v_cvt_pk_f32_fp8_sdwa v[116:117], v117 src0_sel:WORD_1
	v_pk_fma_f32 v[126:127], v[188:189], v[126:127], v[156:157] op_sel_hi:[0,1,1]
	v_pk_fma_f32 v[156:157], v[188:189], v[186:187], v[194:195] op_sel_hi:[0,1,1]
	v_pk_fma_f32 v[186:187], v[188:189], v[202:203], v[196:197] op_sel_hi:[0,1,1]
	v_pk_fma_f32 v[116:117], v[188:189], v[116:117], v[120:121] op_sel_hi:[0,1,1]
	v_cvt_pk_f32_fp8_e32 v[120:121], v118
	v_cvt_pk_f32_fp8_sdwa v[194:195], v118 src0_sel:WORD_1
	v_cvt_pk_f32_fp8_e32 v[196:197], v119
	v_cvt_pk_f32_fp8_sdwa v[118:119], v119 src0_sel:WORD_1
	v_pk_fma_f32 v[120:121], v[188:189], v[120:121], v[124:125] op_sel_hi:[0,1,1]
	v_pk_fma_f32 v[124:125], v[188:189], v[194:195], v[198:199] op_sel_hi:[0,1,1]
	v_pk_fma_f32 v[194:195], v[188:189], v[196:197], v[200:201] op_sel_hi:[0,1,1]
	v_pk_fma_f32 v[118:119], v[188:189], v[118:119], v[122:123] op_sel_hi:[0,1,1]
	v_mov_b32_e32 v122, v189
	s_waitcnt vmcnt(29)
	v_cvt_pk_f32_fp8_e32 v[188:189], v112
	v_cvt_pk_f32_fp8_sdwa v[196:197], v112 src0_sel:WORD_1
	v_cvt_pk_f32_fp8_e32 v[198:199], v113
	v_cvt_pk_f32_fp8_sdwa v[112:113], v113 src0_sel:WORD_1
	v_pk_fma_f32 v[126:127], v[122:123], v[188:189], v[126:127] op_sel_hi:[0,1,1]
	v_pk_fma_f32 v[156:157], v[122:123], v[196:197], v[156:157] op_sel_hi:[0,1,1]
	v_cvt_pk_f32_fp8_sdwa v[188:189], v114 src0_sel:WORD_1
	v_pk_fma_f32 v[112:113], v[122:123], v[112:113], v[116:117] op_sel_hi:[0,1,1]
	v_cvt_pk_f32_fp8_e32 v[116:117], v114
	v_cvt_pk_f32_fp8_e32 v[196:197], v115
	v_cvt_pk_f32_fp8_sdwa v[114:115], v115 src0_sel:WORD_1
	v_pk_fma_f32 v[186:187], v[122:123], v[198:199], v[186:187] op_sel_hi:[0,1,1]
	v_pk_fma_f32 v[116:117], v[122:123], v[116:117], v[120:121] op_sel_hi:[0,1,1]
	v_pk_fma_f32 v[120:121], v[122:123], v[188:189], v[124:125] op_sel_hi:[0,1,1]
	v_pk_fma_f32 v[124:125], v[122:123], v[196:197], v[194:195] op_sel_hi:[0,1,1]
	v_pk_fma_f32 v[114:115], v[122:123], v[114:115], v[118:119] op_sel_hi:[0,1,1]
	s_waitcnt vmcnt(28)
	v_cvt_pk_f32_fp8_e32 v[118:119], v108
	v_cvt_pk_f32_fp8_sdwa v[122:123], v108 src0_sel:WORD_1
	v_cvt_pk_f32_fp8_e32 v[188:189], v109
	v_cvt_pk_f32_fp8_sdwa v[108:109], v109 src0_sel:WORD_1
	s_waitcnt lgkmcnt(2)
	v_pk_fma_f32 v[118:119], v[190:191], v[118:119], v[126:127] op_sel_hi:[0,1,1]
	v_pk_fma_f32 v[122:123], v[190:191], v[122:123], v[156:157] op_sel_hi:[0,1,1]
	v_pk_fma_f32 v[126:127], v[190:191], v[188:189], v[186:187] op_sel_hi:[0,1,1]
	v_pk_fma_f32 v[108:109], v[190:191], v[108:109], v[112:113] op_sel_hi:[0,1,1]
	v_cvt_pk_f32_fp8_e32 v[112:113], v110
	v_cvt_pk_f32_fp8_sdwa v[156:157], v110 src0_sel:WORD_1
	v_cvt_pk_f32_fp8_e32 v[186:187], v111
	v_cvt_pk_f32_fp8_sdwa v[110:111], v111 src0_sel:WORD_1
	v_pk_fma_f32 v[112:113], v[190:191], v[112:113], v[116:117] op_sel_hi:[0,1,1]
	v_pk_fma_f32 v[116:117], v[190:191], v[156:157], v[120:121] op_sel_hi:[0,1,1]
	v_pk_fma_f32 v[120:121], v[190:191], v[186:187], v[124:125] op_sel_hi:[0,1,1]
	v_pk_fma_f32 v[110:111], v[190:191], v[110:111], v[114:115] op_sel_hi:[0,1,1]
	s_waitcnt vmcnt(27)
	v_cvt_pk_f32_fp8_e32 v[114:115], v104
	v_cvt_pk_f32_fp8_sdwa v[124:125], v104 src0_sel:WORD_1
	v_cvt_pk_f32_fp8_e32 v[156:157], v105
	v_cvt_pk_f32_fp8_sdwa v[104:105], v105 src0_sel:WORD_1
	v_pk_fma_f32 v[114:115], v[190:191], v[114:115], v[118:119] op_sel:[1,0,0]
	v_pk_fma_f32 v[118:119], v[190:191], v[124:125], v[122:123] op_sel:[1,0,0]
	v_pk_fma_f32 v[122:123], v[190:191], v[156:157], v[126:127] op_sel:[1,0,0]
	v_pk_fma_f32 v[104:105], v[190:191], v[104:105], v[108:109] op_sel:[1,0,0]
	v_cvt_pk_f32_fp8_e32 v[108:109], v106
	v_cvt_pk_f32_fp8_sdwa v[124:125], v106 src0_sel:WORD_1
	v_cvt_pk_f32_fp8_e32 v[126:127], v107
	v_cvt_pk_f32_fp8_sdwa v[106:107], v107 src0_sel:WORD_1
	v_pk_fma_f32 v[108:109], v[190:191], v[108:109], v[112:113] op_sel:[1,0,0]
	v_pk_fma_f32 v[112:113], v[190:191], v[124:125], v[116:117] op_sel:[1,0,0]
	v_pk_fma_f32 v[116:117], v[190:191], v[126:127], v[120:121] op_sel:[1,0,0]
	v_pk_fma_f32 v[106:107], v[190:191], v[106:107], v[110:111] op_sel:[1,0,0]
	s_waitcnt vmcnt(26)
	v_cvt_pk_f32_fp8_e32 v[110:111], v100
	v_cvt_pk_f32_fp8_sdwa v[120:121], v100 src0_sel:WORD_1
	v_cvt_pk_f32_fp8_e32 v[124:125], v101
	v_cvt_pk_f32_fp8_sdwa v[100:101], v101 src0_sel:WORD_1
	v_pk_fma_f32 v[110:111], v[192:193], v[110:111], v[114:115] op_sel_hi:[0,1,1]
	v_pk_fma_f32 v[114:115], v[192:193], v[120:121], v[118:119] op_sel_hi:[0,1,1]
	v_pk_fma_f32 v[118:119], v[192:193], v[124:125], v[122:123] op_sel_hi:[0,1,1]
	v_pk_fma_f32 v[100:101], v[192:193], v[100:101], v[104:105] op_sel_hi:[0,1,1]
	v_cvt_pk_f32_fp8_e32 v[104:105], v102
	v_cvt_pk_f32_fp8_sdwa v[120:121], v102 src0_sel:WORD_1
	v_cvt_pk_f32_fp8_e32 v[122:123], v103
	v_cvt_pk_f32_fp8_sdwa v[102:103], v103 src0_sel:WORD_1
	v_pk_fma_f32 v[104:105], v[192:193], v[104:105], v[108:109] op_sel_hi:[0,1,1]
	v_pk_fma_f32 v[108:109], v[192:193], v[120:121], v[112:113] op_sel_hi:[0,1,1]
	v_pk_fma_f32 v[112:113], v[192:193], v[122:123], v[116:117] op_sel_hi:[0,1,1]
	s_waitcnt vmcnt(25)
	v_cvt_pk_f32_fp8_e32 v[116:117], v96
	v_cvt_pk_f32_fp8_sdwa v[120:121], v96 src0_sel:WORD_1
	v_cvt_pk_f32_fp8_e32 v[122:123], v97
	v_cvt_pk_f32_fp8_sdwa v[96:97], v97 src0_sel:WORD_1
	v_pk_fma_f32 v[102:103], v[192:193], v[102:103], v[106:107] op_sel_hi:[0,1,1]
	v_mov_b32_e32 v106, v193
	v_pk_fma_f32 v[110:111], v[106:107], v[116:117], v[110:111] op_sel_hi:[0,1,1]
	v_pk_fma_f32 v[114:115], v[106:107], v[120:121], v[114:115] op_sel_hi:[0,1,1]
	v_pk_fma_f32 v[116:117], v[106:107], v[122:123], v[118:119] op_sel_hi:[0,1,1]
	v_pk_fma_f32 v[96:97], v[106:107], v[96:97], v[100:101] op_sel_hi:[0,1,1]
	v_cvt_pk_f32_fp8_e32 v[100:101], v98
	v_cvt_pk_f32_fp8_sdwa v[118:119], v98 src0_sel:WORD_1
	v_cvt_pk_f32_fp8_e32 v[120:121], v99
	v_cvt_pk_f32_fp8_sdwa v[98:99], v99 src0_sel:WORD_1
	v_pk_fma_f32 v[100:101], v[106:107], v[100:101], v[104:105] op_sel_hi:[0,1,1]
	v_pk_fma_f32 v[104:105], v[106:107], v[118:119], v[108:109] op_sel_hi:[0,1,1]
	v_pk_fma_f32 v[108:109], v[106:107], v[120:121], v[112:113] op_sel_hi:[0,1,1]
	v_pk_fma_f32 v[98:99], v[106:107], v[98:99], v[102:103] op_sel_hi:[0,1,1]
	s_waitcnt vmcnt(24)
	v_cvt_pk_f32_fp8_e32 v[102:103], v92
	v_cvt_pk_f32_fp8_sdwa v[106:107], v92 src0_sel:WORD_1
	v_cvt_pk_f32_fp8_e32 v[112:113], v93
	v_cvt_pk_f32_fp8_sdwa v[92:93], v93 src0_sel:WORD_1
	s_waitcnt lgkmcnt(1)
	v_pk_fma_f32 v[102:103], v[132:133], v[102:103], v[110:111] op_sel_hi:[0,1,1]
	v_pk_fma_f32 v[106:107], v[132:133], v[106:107], v[114:115] op_sel_hi:[0,1,1]
	v_pk_fma_f32 v[110:111], v[132:133], v[112:113], v[116:117] op_sel_hi:[0,1,1]
	v_pk_fma_f32 v[92:93], v[132:133], v[92:93], v[96:97] op_sel_hi:[0,1,1]
	v_cvt_pk_f32_fp8_e32 v[96:97], v94
	v_cvt_pk_f32_fp8_sdwa v[112:113], v94 src0_sel:WORD_1
	v_cvt_pk_f32_fp8_e32 v[114:115], v95
	v_cvt_pk_f32_fp8_sdwa v[94:95], v95 src0_sel:WORD_1
	v_pk_fma_f32 v[96:97], v[132:133], v[96:97], v[100:101] op_sel_hi:[0,1,1]
	v_pk_fma_f32 v[100:101], v[132:133], v[112:113], v[104:105] op_sel_hi:[0,1,1]
	v_pk_fma_f32 v[104:105], v[132:133], v[114:115], v[108:109] op_sel_hi:[0,1,1]
	v_pk_fma_f32 v[94:95], v[132:133], v[94:95], v[98:99] op_sel_hi:[0,1,1]
	s_waitcnt vmcnt(23)
	v_cvt_pk_f32_fp8_e32 v[98:99], v88
	v_cvt_pk_f32_fp8_sdwa v[108:109], v88 src0_sel:WORD_1
	v_cvt_pk_f32_fp8_e32 v[112:113], v89
	v_cvt_pk_f32_fp8_sdwa v[88:89], v89 src0_sel:WORD_1
	v_pk_fma_f32 v[98:99], v[132:133], v[98:99], v[102:103] op_sel:[1,0,0]
	v_pk_fma_f32 v[102:103], v[132:133], v[108:109], v[106:107] op_sel:[1,0,0]
	v_pk_fma_f32 v[106:107], v[132:133], v[112:113], v[110:111] op_sel:[1,0,0]
	v_pk_fma_f32 v[88:89], v[132:133], v[88:89], v[92:93] op_sel:[1,0,0]
	v_cvt_pk_f32_fp8_e32 v[92:93], v90
	v_cvt_pk_f32_fp8_sdwa v[108:109], v90 src0_sel:WORD_1
	v_cvt_pk_f32_fp8_e32 v[110:111], v91
	v_cvt_pk_f32_fp8_sdwa v[90:91], v91 src0_sel:WORD_1
	v_pk_fma_f32 v[92:93], v[132:133], v[92:93], v[96:97] op_sel:[1,0,0]
	v_pk_fma_f32 v[96:97], v[132:133], v[108:109], v[100:101] op_sel:[1,0,0]
	v_pk_fma_f32 v[100:101], v[132:133], v[110:111], v[104:105] op_sel:[1,0,0]
	v_pk_fma_f32 v[90:91], v[132:133], v[90:91], v[94:95] op_sel:[1,0,0]
	s_waitcnt vmcnt(22)
	v_cvt_pk_f32_fp8_e32 v[94:95], v84
	v_cvt_pk_f32_fp8_sdwa v[104:105], v84 src0_sel:WORD_1
	v_cvt_pk_f32_fp8_e32 v[108:109], v85
	v_cvt_pk_f32_fp8_sdwa v[84:85], v85 src0_sel:WORD_1
	v_pk_fma_f32 v[94:95], v[134:135], v[94:95], v[98:99] op_sel_hi:[0,1,1]
	v_pk_fma_f32 v[98:99], v[134:135], v[104:105], v[102:103] op_sel_hi:[0,1,1]
	v_pk_fma_f32 v[102:103], v[134:135], v[108:109], v[106:107] op_sel_hi:[0,1,1]
	v_pk_fma_f32 v[84:85], v[134:135], v[84:85], v[88:89] op_sel_hi:[0,1,1]
	v_cvt_pk_f32_fp8_e32 v[88:89], v86
	v_cvt_pk_f32_fp8_sdwa v[104:105], v86 src0_sel:WORD_1
	v_cvt_pk_f32_fp8_e32 v[106:107], v87
	v_cvt_pk_f32_fp8_sdwa v[86:87], v87 src0_sel:WORD_1
	v_pk_fma_f32 v[88:89], v[134:135], v[88:89], v[92:93] op_sel_hi:[0,1,1]
	v_pk_fma_f32 v[92:93], v[134:135], v[104:105], v[96:97] op_sel_hi:[0,1,1]
	v_pk_fma_f32 v[96:97], v[134:135], v[106:107], v[100:101] op_sel_hi:[0,1,1]
	s_waitcnt vmcnt(21)
	v_cvt_pk_f32_fp8_e32 v[100:101], v80
	v_cvt_pk_f32_fp8_sdwa v[104:105], v80 src0_sel:WORD_1
	v_cvt_pk_f32_fp8_e32 v[106:107], v81
	v_cvt_pk_f32_fp8_sdwa v[80:81], v81 src0_sel:WORD_1
	v_pk_fma_f32 v[86:87], v[134:135], v[86:87], v[90:91] op_sel_hi:[0,1,1]
	v_mov_b32_e32 v90, v135
	v_pk_fma_f32 v[94:95], v[90:91], v[100:101], v[94:95] op_sel_hi:[0,1,1]
	v_pk_fma_f32 v[98:99], v[90:91], v[104:105], v[98:99] op_sel_hi:[0,1,1]
	v_pk_fma_f32 v[100:101], v[90:91], v[106:107], v[102:103] op_sel_hi:[0,1,1]
	v_pk_fma_f32 v[80:81], v[90:91], v[80:81], v[84:85] op_sel_hi:[0,1,1]
	v_cvt_pk_f32_fp8_e32 v[84:85], v82
	v_cvt_pk_f32_fp8_sdwa v[102:103], v82 src0_sel:WORD_1
	v_cvt_pk_f32_fp8_e32 v[104:105], v83
	v_cvt_pk_f32_fp8_sdwa v[82:83], v83 src0_sel:WORD_1
	v_pk_fma_f32 v[84:85], v[90:91], v[84:85], v[88:89] op_sel_hi:[0,1,1]
	v_pk_fma_f32 v[88:89], v[90:91], v[102:103], v[92:93] op_sel_hi:[0,1,1]
	v_pk_fma_f32 v[92:93], v[90:91], v[104:105], v[96:97] op_sel_hi:[0,1,1]
	v_pk_fma_f32 v[82:83], v[90:91], v[82:83], v[86:87] op_sel_hi:[0,1,1]
	s_waitcnt vmcnt(20)
	v_cvt_pk_f32_fp8_e32 v[86:87], v76
	v_cvt_pk_f32_fp8_sdwa v[90:91], v76 src0_sel:WORD_1
	v_cvt_pk_f32_fp8_e32 v[96:97], v77
	v_cvt_pk_f32_fp8_sdwa v[76:77], v77 src0_sel:WORD_1
	s_waitcnt lgkmcnt(0)
	v_pk_fma_f32 v[86:87], v[128:129], v[86:87], v[94:95] op_sel_hi:[0,1,1]
	v_pk_fma_f32 v[90:91], v[128:129], v[90:91], v[98:99] op_sel_hi:[0,1,1]
	v_pk_fma_f32 v[94:95], v[128:129], v[96:97], v[100:101] op_sel_hi:[0,1,1]
	v_pk_fma_f32 v[76:77], v[128:129], v[76:77], v[80:81] op_sel_hi:[0,1,1]
	v_cvt_pk_f32_fp8_e32 v[80:81], v78
	v_cvt_pk_f32_fp8_sdwa v[96:97], v78 src0_sel:WORD_1
	v_cvt_pk_f32_fp8_e32 v[98:99], v79
	v_cvt_pk_f32_fp8_sdwa v[78:79], v79 src0_sel:WORD_1
	v_pk_fma_f32 v[80:81], v[128:129], v[80:81], v[84:85] op_sel_hi:[0,1,1]
	v_pk_fma_f32 v[84:85], v[128:129], v[96:97], v[88:89] op_sel_hi:[0,1,1]
	v_pk_fma_f32 v[88:89], v[128:129], v[98:99], v[92:93] op_sel_hi:[0,1,1]
	v_pk_fma_f32 v[78:79], v[128:129], v[78:79], v[82:83] op_sel_hi:[0,1,1]
	s_waitcnt vmcnt(19)
	v_cvt_pk_f32_fp8_e32 v[82:83], v72
	v_cvt_pk_f32_fp8_sdwa v[92:93], v72 src0_sel:WORD_1
	v_cvt_pk_f32_fp8_e32 v[96:97], v73
	v_cvt_pk_f32_fp8_sdwa v[72:73], v73 src0_sel:WORD_1
	v_pk_fma_f32 v[82:83], v[128:129], v[82:83], v[86:87] op_sel:[1,0,0]
	v_pk_fma_f32 v[86:87], v[128:129], v[92:93], v[90:91] op_sel:[1,0,0]
	v_pk_fma_f32 v[90:91], v[128:129], v[96:97], v[94:95] op_sel:[1,0,0]
	v_pk_fma_f32 v[72:73], v[128:129], v[72:73], v[76:77] op_sel:[1,0,0]
	v_cvt_pk_f32_fp8_e32 v[76:77], v74
	v_cvt_pk_f32_fp8_sdwa v[92:93], v74 src0_sel:WORD_1
	v_cvt_pk_f32_fp8_e32 v[94:95], v75
	v_cvt_pk_f32_fp8_sdwa v[74:75], v75 src0_sel:WORD_1
	v_pk_fma_f32 v[76:77], v[128:129], v[76:77], v[80:81] op_sel:[1,0,0]
	v_pk_fma_f32 v[80:81], v[128:129], v[92:93], v[84:85] op_sel:[1,0,0]
	v_pk_fma_f32 v[84:85], v[128:129], v[94:95], v[88:89] op_sel:[1,0,0]
	v_pk_fma_f32 v[74:75], v[128:129], v[74:75], v[78:79] op_sel:[1,0,0]
	s_waitcnt vmcnt(18)
	v_cvt_pk_f32_fp8_e32 v[78:79], v68
	v_cvt_pk_f32_fp8_sdwa v[88:89], v68 src0_sel:WORD_1
	v_cvt_pk_f32_fp8_e32 v[92:93], v69
	v_cvt_pk_f32_fp8_sdwa v[68:69], v69 src0_sel:WORD_1
	v_pk_fma_f32 v[78:79], v[130:131], v[78:79], v[82:83] op_sel_hi:[0,1,1]
	v_pk_fma_f32 v[82:83], v[130:131], v[88:89], v[86:87] op_sel_hi:[0,1,1]
	v_pk_fma_f32 v[86:87], v[130:131], v[92:93], v[90:91] op_sel_hi:[0,1,1]
	v_pk_fma_f32 v[68:69], v[130:131], v[68:69], v[72:73] op_sel_hi:[0,1,1]
	v_cvt_pk_f32_fp8_e32 v[72:73], v70
	v_cvt_pk_f32_fp8_sdwa v[88:89], v70 src0_sel:WORD_1
	v_cvt_pk_f32_fp8_e32 v[90:91], v71
	v_cvt_pk_f32_fp8_sdwa v[70:71], v71 src0_sel:WORD_1
	v_pk_fma_f32 v[72:73], v[130:131], v[72:73], v[76:77] op_sel_hi:[0,1,1]
	v_pk_fma_f32 v[76:77], v[130:131], v[88:89], v[80:81] op_sel_hi:[0,1,1]
	v_pk_fma_f32 v[80:81], v[130:131], v[90:91], v[84:85] op_sel_hi:[0,1,1]
	s_waitcnt vmcnt(17)
	v_cvt_pk_f32_fp8_e32 v[84:85], v64
	v_cvt_pk_f32_fp8_sdwa v[88:89], v64 src0_sel:WORD_1
	v_cvt_pk_f32_fp8_e32 v[90:91], v65
	v_cvt_pk_f32_fp8_sdwa v[64:65], v65 src0_sel:WORD_1
	v_pk_fma_f32 v[70:71], v[130:131], v[70:71], v[74:75] op_sel_hi:[0,1,1]
	v_mov_b32_e32 v74, v131
	v_pk_fma_f32 v[78:79], v[74:75], v[84:85], v[78:79] op_sel_hi:[0,1,1]
	v_pk_fma_f32 v[64:65], v[74:75], v[64:65], v[68:69] op_sel_hi:[0,1,1]
	v_cvt_pk_f32_fp8_e32 v[68:69], v66
	v_pk_fma_f32 v[82:83], v[74:75], v[88:89], v[82:83] op_sel_hi:[0,1,1]
	v_pk_fma_f32 v[84:85], v[74:75], v[90:91], v[86:87] op_sel_hi:[0,1,1]
	v_cvt_pk_f32_fp8_sdwa v[86:87], v66 src0_sel:WORD_1
	v_cvt_pk_f32_fp8_e32 v[88:89], v67
	v_cvt_pk_f32_fp8_sdwa v[66:67], v67 src0_sel:WORD_1
	v_pk_fma_f32 v[68:69], v[74:75], v[68:69], v[72:73] op_sel_hi:[0,1,1]
	v_pk_fma_f32 v[72:73], v[74:75], v[86:87], v[76:77] op_sel_hi:[0,1,1]
	v_pk_fma_f32 v[76:77], v[74:75], v[88:89], v[80:81] op_sel_hi:[0,1,1]
	v_pk_fma_f32 v[66:67], v[74:75], v[66:67], v[70:71] op_sel_hi:[0,1,1]
	v_cndmask_b32_e64 v70, v68, v78, s[8:9]
	v_cndmask_b32_e64 v68, v78, v68, s[8:9]
	ds_bpermute_b32 v68, v137, v68
	v_cndmask_b32_e64 v71, v79, v69, s[8:9]
	ds_bpermute_b32 v71, v137, v71
	v_cndmask_b32_e64 v74, v82, v72, s[8:9]
	ds_bpermute_b32 v74, v137, v74
	s_waitcnt lgkmcnt(2)
	v_add_f32_e32 v68, v70, v68
	v_cndmask_b32_e64 v69, v69, v79, s[8:9]
	v_cndmask_b32_e64 v70, v72, v82, s[8:9]
	v_cndmask_b32_e64 v72, v83, v73, s[8:9]
	s_waitcnt lgkmcnt(1)
	v_add_f32_e32 v69, v69, v71
	v_cndmask_b32_e64 v71, v73, v83, s[8:9]
	ds_bpermute_b32 v72, v137, v72
	v_cndmask_b32_e64 v73, v84, v76, s[8:9]
	s_waitcnt lgkmcnt(1)
	v_add_f32_e32 v70, v70, v74
	ds_bpermute_b32 v73, v137, v73
	v_cndmask_b32_e64 v74, v85, v77, s[8:9]
	ds_bpermute_b32 v74, v137, v74
	s_waitcnt lgkmcnt(2)
	v_add_f32_e32 v71, v71, v72
	v_cndmask_b32_e64 v72, v76, v84, s[8:9]
	s_waitcnt lgkmcnt(1)
	v_add_f32_e32 v72, v72, v73
	v_cndmask_b32_e64 v73, v77, v85, s[8:9]
	s_waitcnt lgkmcnt(0)
	v_add_f32_e32 v73, v73, v74
	v_cndmask_b32_e64 v74, v66, v64, s[8:9]
	v_cndmask_b32_e64 v64, v64, v66, s[8:9]
	v_cndmask_b32_e64 v66, v65, v67, s[8:9]
	ds_bpermute_b32 v64, v137, v64
	ds_bpermute_b32 v66, v137, v66
	v_cndmask_b32_e64 v65, v67, v65, s[8:9]
	v_cndmask_b32_e64 v75, v68, v72, s[10:11]
	v_cndmask_b32_e64 v67, v73, v69, s[10:11]
	s_waitcnt lgkmcnt(1)
	v_add_f32_e32 v64, v74, v64
	s_waitcnt lgkmcnt(0)
	v_add_f32_e32 v65, v65, v66
	v_cndmask_b32_e64 v66, v72, v68, s[10:11]
	v_cndmask_b32_e64 v68, v69, v73, s[10:11]
	v_cndmask_b32_e64 v69, v70, v64, s[10:11]
	v_cndmask_b32_e64 v72, v71, v65, s[10:11]
	ds_bpermute_b32 v75, v138, v75
	ds_bpermute_b32 v68, v138, v68
	ds_bpermute_b32 v69, v138, v69
	ds_bpermute_b32 v72, v138, v72
	v_cndmask_b32_e64 v64, v64, v70, s[10:11]
	v_cndmask_b32_e64 v65, v65, v71, s[10:11]
	s_waitcnt lgkmcnt(3)
	v_add_f32_e32 v66, v66, v75
	s_waitcnt lgkmcnt(2)
	v_add_f32_e32 v67, v67, v68
	s_waitcnt lgkmcnt(1)
	v_add_f32_e32 v64, v64, v69
	s_waitcnt lgkmcnt(0)
	v_add_f32_e32 v65, v65, v72
	v_cndmask_b32_e64 v68, v66, v64, s[12:13]
	v_cndmask_b32_e64 v69, v67, v65, s[12:13]
	s_or_b32 s56, s56, s2
	ds_bpermute_b32 v68, v136, v68
	ds_bpermute_b32 v69, v136, v69
	s_ashr_i32 s57, s56, 31
	s_lshl_b64 s[56:57], s[56:57], 13
	s_add_u32 s56, s64, s56
	s_addc_u32 s57, s65, s57
	s_lshl_b32 s55, s55, 8
	v_cndmask_b32_e64 v64, v64, v66, s[12:13]
	v_cndmask_b32_e64 v65, v65, v67, s[12:13]
	s_add_u32 s56, s56, s55
	s_waitcnt lgkmcnt(1)
	v_add_f32_e32 v64, v64, v68
	s_waitcnt lgkmcnt(0)
	v_add_f32_e32 v65, v65, v69
	s_addc_u32 s57, s57, 0
	v_cvt_pk_bf16_f32 v66, v64, v65
	v_lshl_add_u64 v[64:65], s[56:57], 0, v[140:141]
	v_lshl_add_u64 v[64:65], v[64:65], 0, v[154:155]
	global_store_dword v[64:65], v66, off nt
	s_add_i32 s3, s3, 16
	s_add_i32 s22, s22, 0x80000
	s_add_i32 s53, s53, 32
	s_and_b64 vcc, exec, s[30:31]
	s_cbranch_vccnz .LBB0_841
.LBB0_839:
	s_and_b32 s30, s54, 6
	s_or_b32 s56, s30, 1
	v_lshl_or_b32 v139, s56, 7, v163
	v_lshl_add_u32 v68, v139, 1, s34
	ds_read_b128 v[64:67], v68
	s_lshr_b32 s55, s54, 3
	s_lshl_b32 s31, s55, 21
	s_add_u32 s58, s14, s31
	s_addc_u32 s59, s15, 0
	s_waitcnt lgkmcnt(0)
	v_lshlrev_b32_e32 v72, 7, v64
	v_bfe_u32 v64, v64, 16, 16
	v_and_or_b32 v72, v72, s36, v142
	v_lshl_or_b32 v64, v64, 7, v142
	ds_read_b128 v[68:71], v68 offset:16
	global_load_dwordx4 v[124:127], v72, s[58:59]
	global_load_dwordx4 v[120:123], v64, s[58:59]
	v_lshlrev_b32_e32 v64, 7, v65
	v_bfe_u32 v65, v65, 16, 16
	v_and_or_b32 v64, v64, s36, v142
	v_lshl_or_b32 v65, v65, 7, v142
	global_load_dwordx4 v[116:119], v64, s[58:59]
	global_load_dwordx4 v[112:115], v65, s[58:59]
	v_lshlrev_b32_e32 v64, 7, v66
	v_bfe_u32 v65, v66, 16, 16
	v_and_or_b32 v64, v64, s36, v142
	v_lshl_or_b32 v65, v65, 7, v142
	global_load_dwordx4 v[108:111], v64, s[58:59]
	global_load_dwordx4 v[104:107], v65, s[58:59]
	v_lshlrev_b32_e32 v64, 7, v67
	v_bfe_u32 v65, v67, 16, 16
	v_and_or_b32 v64, v64, s36, v142
	v_lshl_or_b32 v65, v65, 7, v142
	global_load_dwordx4 v[100:103], v64, s[58:59]
	global_load_dwordx4 v[96:99], v65, s[58:59]
	s_waitcnt lgkmcnt(0)
	v_lshlrev_b32_e32 v64, 7, v68
	v_bfe_u32 v65, v68, 16, 16
	v_and_or_b32 v64, v64, s36, v142
	v_lshl_or_b32 v65, v65, 7, v142
	global_load_dwordx4 v[92:95], v64, s[58:59]
	global_load_dwordx4 v[88:91], v65, s[58:59]
	v_lshlrev_b32_e32 v64, 7, v69
	v_bfe_u32 v65, v69, 16, 16
	v_and_or_b32 v64, v64, s36, v142
	v_lshl_or_b32 v65, v65, 7, v142
	global_load_dwordx4 v[84:87], v64, s[58:59]
	global_load_dwordx4 v[80:83], v65, s[58:59]
	v_lshlrev_b32_e32 v64, 7, v70
	v_bfe_u32 v65, v70, 16, 16
	v_and_or_b32 v64, v64, s36, v142
	v_lshl_or_b32 v65, v65, 7, v142
	global_load_dwordx4 v[76:79], v64, s[58:59]
	global_load_dwordx4 v[72:75], v65, s[58:59]
	v_lshlrev_b32_e32 v64, 7, v71
	v_bfe_u32 v65, v71, 16, 16
	v_and_or_b32 v64, v64, s36, v142
	v_lshl_or_b32 v65, v65, 7, v142
	global_load_dwordx4 v[68:71], v64, s[58:59]
	s_nop 0
	global_load_dwordx4 v[64:67], v65, s[58:59]
	s_waitcnt vmcnt(31)
	v_cvt_pk_f32_fp8_e32 v[156:157], v0
	v_cvt_pk_f32_fp8_sdwa v[194:195], v0 src0_sel:WORD_1
	v_cvt_pk_f32_fp8_e32 v[196:197], v1
	v_cvt_pk_f32_fp8_sdwa v[198:199], v1 src0_sel:WORD_1
	v_lshl_add_u32 v128, s30, 9, v164
	s_waitcnt vmcnt(30)
	v_cvt_pk_f32_fp8_e32 v[208:209], v4
	v_cvt_pk_f32_fp8_sdwa v[210:211], v4 src0_sel:WORD_1
	v_cvt_pk_f32_fp8_e32 v[212:213], v5
	v_cvt_pk_f32_fp8_sdwa v[214:215], v5 src0_sel:WORD_1
	ds_read_b128 v[186:189], v128 offset:2048
	ds_read_b128 v[190:193], v128 offset:2064
	ds_read_b128 v[132:135], v128 offset:2080
	ds_read_b128 v[128:131], v128 offset:2096
	v_cvt_pk_f32_fp8_e32 v[200:201], v2
	s_waitcnt lgkmcnt(3)
	v_pk_fma_f32 v[156:157], v[186:187], v[156:157], 0 op_sel_hi:[0,1,0]
	v_pk_fma_f32 v[194:195], v[186:187], v[194:195], 0 op_sel_hi:[0,1,0]
	v_pk_fma_f32 v[196:197], v[186:187], v[196:197], 0 op_sel_hi:[0,1,0]
	v_pk_fma_f32 v[198:199], v[186:187], v[198:199], 0 op_sel_hi:[0,1,0]
	v_cvt_pk_f32_fp8_sdwa v[202:203], v2 src0_sel:WORD_1
	v_cvt_pk_f32_fp8_e32 v[204:205], v3
	v_cvt_pk_f32_fp8_sdwa v[206:207], v3 src0_sel:WORD_1
	v_pk_fma_f32 v[156:157], v[186:187], v[208:209], v[156:157] op_sel:[1,0,0]
	v_pk_fma_f32 v[194:195], v[186:187], v[210:211], v[194:195] op_sel:[1,0,0]
	v_pk_fma_f32 v[196:197], v[186:187], v[212:213], v[196:197] op_sel:[1,0,0]
	v_pk_fma_f32 v[198:199], v[186:187], v[214:215], v[198:199] op_sel:[1,0,0]
	v_cvt_pk_f32_fp8_e32 v[208:209], v6
	v_cvt_pk_f32_fp8_sdwa v[210:211], v6 src0_sel:WORD_1
	v_cvt_pk_f32_fp8_e32 v[212:213], v7
	v_cvt_pk_f32_fp8_sdwa v[214:215], v7 src0_sel:WORD_1
	v_pk_fma_f32 v[200:201], v[186:187], v[200:201], 0 op_sel_hi:[0,1,0]
	v_pk_fma_f32 v[202:203], v[186:187], v[202:203], 0 op_sel_hi:[0,1,0]
	v_pk_fma_f32 v[204:205], v[186:187], v[204:205], 0 op_sel_hi:[0,1,0]
	v_pk_fma_f32 v[206:207], v[186:187], v[206:207], 0 op_sel_hi:[0,1,0]
	v_pk_fma_f32 v[200:201], v[186:187], v[208:209], v[200:201] op_sel:[1,0,0]
	v_pk_fma_f32 v[202:203], v[186:187], v[210:211], v[202:203] op_sel:[1,0,0]
	v_pk_fma_f32 v[204:205], v[186:187], v[212:213], v[204:205] op_sel:[1,0,0]
	v_pk_fma_f32 v[186:187], v[186:187], v[214:215], v[206:207] op_sel:[1,0,0]
	s_waitcnt vmcnt(29)
	v_cvt_pk_f32_fp8_e32 v[206:207], v8
	v_cvt_pk_f32_fp8_sdwa v[208:209], v8 src0_sel:WORD_1
	v_cvt_pk_f32_fp8_e32 v[210:211], v9
	v_cvt_pk_f32_fp8_sdwa v[212:213], v9 src0_sel:WORD_1
	v_pk_fma_f32 v[156:157], v[188:189], v[206:207], v[156:157] op_sel_hi:[0,1,1]
	v_pk_fma_f32 v[194:195], v[188:189], v[208:209], v[194:195] op_sel_hi:[0,1,1]
	v_pk_fma_f32 v[196:197], v[188:189], v[210:211], v[196:197] op_sel_hi:[0,1,1]
	v_pk_fma_f32 v[198:199], v[188:189], v[212:213], v[198:199] op_sel_hi:[0,1,1]
	v_cvt_pk_f32_fp8_e32 v[206:207], v10
	v_cvt_pk_f32_fp8_sdwa v[208:209], v10 src0_sel:WORD_1
	v_cvt_pk_f32_fp8_e32 v[210:211], v11
	v_cvt_pk_f32_fp8_sdwa v[212:213], v11 src0_sel:WORD_1
	v_pk_fma_f32 v[200:201], v[188:189], v[206:207], v[200:201] op_sel_hi:[0,1,1]
	v_pk_fma_f32 v[202:203], v[188:189], v[208:209], v[202:203] op_sel_hi:[0,1,1]
	v_pk_fma_f32 v[204:205], v[188:189], v[210:211], v[204:205] op_sel_hi:[0,1,1]
	v_pk_fma_f32 v[186:187], v[188:189], v[212:213], v[186:187] op_sel_hi:[0,1,1]
	v_mov_b32_e32 v140, v189
	s_waitcnt vmcnt(28)
	v_cvt_pk_f32_fp8_e32 v[188:189], v12
	v_cvt_pk_f32_fp8_sdwa v[206:207], v12 src0_sel:WORD_1
	v_cvt_pk_f32_fp8_e32 v[208:209], v13
	v_cvt_pk_f32_fp8_sdwa v[210:211], v13 src0_sel:WORD_1
	v_pk_fma_f32 v[156:157], v[140:141], v[188:189], v[156:157] op_sel_hi:[0,1,1]
	v_pk_fma_f32 v[188:189], v[140:141], v[206:207], v[194:195] op_sel_hi:[0,1,1]
	v_pk_fma_f32 v[194:195], v[140:141], v[208:209], v[196:197] op_sel_hi:[0,1,1]
	v_pk_fma_f32 v[196:197], v[140:141], v[210:211], v[198:199] op_sel_hi:[0,1,1]
	v_cvt_pk_f32_fp8_e32 v[198:199], v14
	v_cvt_pk_f32_fp8_sdwa v[206:207], v14 src0_sel:WORD_1
	v_cvt_pk_f32_fp8_e32 v[208:209], v15
	v_cvt_pk_f32_fp8_sdwa v[210:211], v15 src0_sel:WORD_1
	v_pk_fma_f32 v[198:199], v[140:141], v[198:199], v[200:201] op_sel_hi:[0,1,1]
	v_pk_fma_f32 v[200:201], v[140:141], v[206:207], v[202:203] op_sel_hi:[0,1,1]
	v_pk_fma_f32 v[202:203], v[140:141], v[208:209], v[204:205] op_sel_hi:[0,1,1]
	v_pk_fma_f32 v[186:187], v[140:141], v[210:211], v[186:187] op_sel_hi:[0,1,1]
	s_waitcnt vmcnt(27)
	v_cvt_pk_f32_fp8_e32 v[204:205], v16
	v_cvt_pk_f32_fp8_sdwa v[206:207], v16 src0_sel:WORD_1
	v_cvt_pk_f32_fp8_e32 v[208:209], v17
	v_cvt_pk_f32_fp8_sdwa v[210:211], v17 src0_sel:WORD_1
	s_waitcnt lgkmcnt(2)
	v_pk_fma_f32 v[156:157], v[190:191], v[204:205], v[156:157] op_sel_hi:[0,1,1]
	v_pk_fma_f32 v[188:189], v[190:191], v[206:207], v[188:189] op_sel_hi:[0,1,1]
	v_pk_fma_f32 v[194:195], v[190:191], v[208:209], v[194:195] op_sel_hi:[0,1,1]
	v_pk_fma_f32 v[196:197], v[190:191], v[210:211], v[196:197] op_sel_hi:[0,1,1]
	v_cvt_pk_f32_fp8_e32 v[204:205], v18
	v_cvt_pk_f32_fp8_sdwa v[206:207], v18 src0_sel:WORD_1
	v_cvt_pk_f32_fp8_e32 v[208:209], v19
	v_cvt_pk_f32_fp8_sdwa v[210:211], v19 src0_sel:WORD_1
	v_pk_fma_f32 v[198:199], v[190:191], v[204:205], v[198:199] op_sel_hi:[0,1,1]
	v_pk_fma_f32 v[200:201], v[190:191], v[206:207], v[200:201] op_sel_hi:[0,1,1]
	v_pk_fma_f32 v[202:203], v[190:191], v[208:209], v[202:203] op_sel_hi:[0,1,1]
	v_pk_fma_f32 v[186:187], v[190:191], v[210:211], v[186:187] op_sel_hi:[0,1,1]
	s_waitcnt vmcnt(26)
	v_cvt_pk_f32_fp8_e32 v[204:205], v20
	v_cvt_pk_f32_fp8_sdwa v[206:207], v20 src0_sel:WORD_1
	v_cvt_pk_f32_fp8_e32 v[208:209], v21
	v_cvt_pk_f32_fp8_sdwa v[210:211], v21 src0_sel:WORD_1
	v_pk_fma_f32 v[156:157], v[190:191], v[204:205], v[156:157] op_sel:[1,0,0]
	v_pk_fma_f32 v[188:189], v[190:191], v[206:207], v[188:189] op_sel:[1,0,0]
	v_pk_fma_f32 v[194:195], v[190:191], v[208:209], v[194:195] op_sel:[1,0,0]
	v_pk_fma_f32 v[196:197], v[190:191], v[210:211], v[196:197] op_sel:[1,0,0]
	v_cvt_pk_f32_fp8_e32 v[204:205], v22
	v_cvt_pk_f32_fp8_sdwa v[206:207], v22 src0_sel:WORD_1
	v_cvt_pk_f32_fp8_e32 v[208:209], v23
	v_cvt_pk_f32_fp8_sdwa v[210:211], v23 src0_sel:WORD_1
	v_pk_fma_f32 v[198:199], v[190:191], v[204:205], v[198:199] op_sel:[1,0,0]
	v_pk_fma_f32 v[200:201], v[190:191], v[206:207], v[200:201] op_sel:[1,0,0]
	v_pk_fma_f32 v[202:203], v[190:191], v[208:209], v[202:203] op_sel:[1,0,0]
	v_pk_fma_f32 v[186:187], v[190:191], v[210:211], v[186:187] op_sel:[1,0,0]
	s_waitcnt vmcnt(25)
	v_cvt_pk_f32_fp8_e32 v[190:191], v24
	v_cvt_pk_f32_fp8_sdwa v[204:205], v24 src0_sel:WORD_1
	v_cvt_pk_f32_fp8_e32 v[206:207], v25
	v_cvt_pk_f32_fp8_sdwa v[208:209], v25 src0_sel:WORD_1
	v_pk_fma_f32 v[156:157], v[192:193], v[190:191], v[156:157] op_sel_hi:[0,1,1]
	v_pk_fma_f32 v[188:189], v[192:193], v[204:205], v[188:189] op_sel_hi:[0,1,1]
	v_pk_fma_f32 v[190:191], v[192:193], v[206:207], v[194:195] op_sel_hi:[0,1,1]
	v_pk_fma_f32 v[194:195], v[192:193], v[208:209], v[196:197] op_sel_hi:[0,1,1]
	v_cvt_pk_f32_fp8_e32 v[196:197], v26
	v_cvt_pk_f32_fp8_sdwa v[204:205], v26 src0_sel:WORD_1
	v_cvt_pk_f32_fp8_e32 v[206:207], v27
	v_cvt_pk_f32_fp8_sdwa v[208:209], v27 src0_sel:WORD_1
	v_pk_fma_f32 v[196:197], v[192:193], v[196:197], v[198:199] op_sel_hi:[0,1,1]
	v_pk_fma_f32 v[198:199], v[192:193], v[204:205], v[200:201] op_sel_hi:[0,1,1]
	v_pk_fma_f32 v[200:201], v[192:193], v[206:207], v[202:203] op_sel_hi:[0,1,1]
	v_pk_fma_f32 v[186:187], v[192:193], v[208:209], v[186:187] op_sel_hi:[0,1,1]
	v_mov_b32_e32 v140, v193
	s_waitcnt vmcnt(24)
	v_cvt_pk_f32_fp8_e32 v[192:193], v28
	v_cvt_pk_f32_fp8_sdwa v[202:203], v28 src0_sel:WORD_1
	v_cvt_pk_f32_fp8_e32 v[204:205], v29
	v_cvt_pk_f32_fp8_sdwa v[206:207], v29 src0_sel:WORD_1
	v_pk_fma_f32 v[156:157], v[140:141], v[192:193], v[156:157] op_sel_hi:[0,1,1]
	v_pk_fma_f32 v[188:189], v[140:141], v[202:203], v[188:189] op_sel_hi:[0,1,1]
	v_pk_fma_f32 v[190:191], v[140:141], v[204:205], v[190:191] op_sel_hi:[0,1,1]
	v_pk_fma_f32 v[192:193], v[140:141], v[206:207], v[194:195] op_sel_hi:[0,1,1]
	v_cvt_pk_f32_fp8_e32 v[194:195], v30
	v_cvt_pk_f32_fp8_sdwa v[202:203], v30 src0_sel:WORD_1
	v_cvt_pk_f32_fp8_e32 v[204:205], v31
	v_cvt_pk_f32_fp8_sdwa v[206:207], v31 src0_sel:WORD_1
	v_pk_fma_f32 v[194:195], v[140:141], v[194:195], v[196:197] op_sel_hi:[0,1,1]
	v_pk_fma_f32 v[196:197], v[140:141], v[202:203], v[198:199] op_sel_hi:[0,1,1]
	v_pk_fma_f32 v[198:199], v[140:141], v[204:205], v[200:201] op_sel_hi:[0,1,1]
	v_pk_fma_f32 v[186:187], v[140:141], v[206:207], v[186:187] op_sel_hi:[0,1,1]
	s_waitcnt vmcnt(23)
	v_cvt_pk_f32_fp8_e32 v[200:201], v32
	v_cvt_pk_f32_fp8_sdwa v[202:203], v32 src0_sel:WORD_1
	v_cvt_pk_f32_fp8_e32 v[204:205], v33
	v_cvt_pk_f32_fp8_sdwa v[206:207], v33 src0_sel:WORD_1
	s_waitcnt lgkmcnt(1)
	v_pk_fma_f32 v[156:157], v[132:133], v[200:201], v[156:157] op_sel_hi:[0,1,1]
	v_pk_fma_f32 v[188:189], v[132:133], v[202:203], v[188:189] op_sel_hi:[0,1,1]
	v_pk_fma_f32 v[190:191], v[132:133], v[204:205], v[190:191] op_sel_hi:[0,1,1]
	v_pk_fma_f32 v[192:193], v[132:133], v[206:207], v[192:193] op_sel_hi:[0,1,1]
	v_cvt_pk_f32_fp8_e32 v[200:201], v34
	v_cvt_pk_f32_fp8_sdwa v[202:203], v34 src0_sel:WORD_1
	v_cvt_pk_f32_fp8_e32 v[204:205], v35
	v_cvt_pk_f32_fp8_sdwa v[206:207], v35 src0_sel:WORD_1
	v_pk_fma_f32 v[194:195], v[132:133], v[200:201], v[194:195] op_sel_hi:[0,1,1]
	v_pk_fma_f32 v[196:197], v[132:133], v[202:203], v[196:197] op_sel_hi:[0,1,1]
	v_pk_fma_f32 v[198:199], v[132:133], v[204:205], v[198:199] op_sel_hi:[0,1,1]
	v_pk_fma_f32 v[186:187], v[132:133], v[206:207], v[186:187] op_sel_hi:[0,1,1]
	s_waitcnt vmcnt(22)
	v_cvt_pk_f32_fp8_e32 v[200:201], v36
	v_cvt_pk_f32_fp8_sdwa v[202:203], v36 src0_sel:WORD_1
	v_cvt_pk_f32_fp8_e32 v[204:205], v37
	v_cvt_pk_f32_fp8_sdwa v[206:207], v37 src0_sel:WORD_1
	v_pk_fma_f32 v[156:157], v[132:133], v[200:201], v[156:157] op_sel:[1,0,0]
	v_pk_fma_f32 v[188:189], v[132:133], v[202:203], v[188:189] op_sel:[1,0,0]
	v_pk_fma_f32 v[190:191], v[132:133], v[204:205], v[190:191] op_sel:[1,0,0]
	v_pk_fma_f32 v[192:193], v[132:133], v[206:207], v[192:193] op_sel:[1,0,0]
	v_cvt_pk_f32_fp8_e32 v[200:201], v38
	v_cvt_pk_f32_fp8_sdwa v[202:203], v38 src0_sel:WORD_1
	v_cvt_pk_f32_fp8_e32 v[204:205], v39
	v_cvt_pk_f32_fp8_sdwa v[206:207], v39 src0_sel:WORD_1
	v_pk_fma_f32 v[194:195], v[132:133], v[200:201], v[194:195] op_sel:[1,0,0]
	v_pk_fma_f32 v[196:197], v[132:133], v[202:203], v[196:197] op_sel:[1,0,0]
	v_pk_fma_f32 v[198:199], v[132:133], v[204:205], v[198:199] op_sel:[1,0,0]
	v_pk_fma_f32 v[132:133], v[132:133], v[206:207], v[186:187] op_sel:[1,0,0]
	s_waitcnt vmcnt(21)
	v_cvt_pk_f32_fp8_e32 v[186:187], v40
	v_cvt_pk_f32_fp8_sdwa v[200:201], v40 src0_sel:WORD_1
	v_cvt_pk_f32_fp8_e32 v[202:203], v41
	v_cvt_pk_f32_fp8_sdwa v[204:205], v41 src0_sel:WORD_1
	v_pk_fma_f32 v[156:157], v[134:135], v[186:187], v[156:157] op_sel_hi:[0,1,1]
	v_pk_fma_f32 v[186:187], v[134:135], v[200:201], v[188:189] op_sel_hi:[0,1,1]
	v_pk_fma_f32 v[188:189], v[134:135], v[202:203], v[190:191] op_sel_hi:[0,1,1]
	v_pk_fma_f32 v[190:191], v[134:135], v[204:205], v[192:193] op_sel_hi:[0,1,1]
	v_cvt_pk_f32_fp8_e32 v[192:193], v42
	v_cvt_pk_f32_fp8_sdwa v[200:201], v42 src0_sel:WORD_1
	v_cvt_pk_f32_fp8_e32 v[202:203], v43
	v_cvt_pk_f32_fp8_sdwa v[204:205], v43 src0_sel:WORD_1
	v_pk_fma_f32 v[192:193], v[134:135], v[192:193], v[194:195] op_sel_hi:[0,1,1]
	v_pk_fma_f32 v[194:195], v[134:135], v[200:201], v[196:197] op_sel_hi:[0,1,1]
	v_pk_fma_f32 v[196:197], v[134:135], v[202:203], v[198:199] op_sel_hi:[0,1,1]
	v_pk_fma_f32 v[132:133], v[134:135], v[204:205], v[132:133] op_sel_hi:[0,1,1]
	s_waitcnt vmcnt(20)
	v_cvt_pk_f32_fp8_e32 v[198:199], v44
	v_cvt_pk_f32_fp8_sdwa v[200:201], v44 src0_sel:WORD_1
	v_cvt_pk_f32_fp8_e32 v[202:203], v45
	v_cvt_pk_f32_fp8_sdwa v[204:205], v45 src0_sel:WORD_1
	v_mov_b32_e32 v134, v135
	v_pk_fma_f32 v[156:157], v[134:135], v[198:199], v[156:157] op_sel_hi:[0,1,1]
	v_pk_fma_f32 v[186:187], v[134:135], v[200:201], v[186:187] op_sel_hi:[0,1,1]
	v_pk_fma_f32 v[188:189], v[134:135], v[202:203], v[188:189] op_sel_hi:[0,1,1]
	v_pk_fma_f32 v[190:191], v[134:135], v[204:205], v[190:191] op_sel_hi:[0,1,1]
	v_cvt_pk_f32_fp8_e32 v[198:199], v46
	v_cvt_pk_f32_fp8_sdwa v[200:201], v46 src0_sel:WORD_1
	v_cvt_pk_f32_fp8_e32 v[202:203], v47
	v_cvt_pk_f32_fp8_sdwa v[204:205], v47 src0_sel:WORD_1
	v_pk_fma_f32 v[192:193], v[134:135], v[198:199], v[192:193] op_sel_hi:[0,1,1]
	v_pk_fma_f32 v[194:195], v[134:135], v[200:201], v[194:195] op_sel_hi:[0,1,1]
	v_pk_fma_f32 v[196:197], v[134:135], v[202:203], v[196:197] op_sel_hi:[0,1,1]
	v_pk_fma_f32 v[132:133], v[134:135], v[204:205], v[132:133] op_sel_hi:[0,1,1]
	s_waitcnt vmcnt(19)
	v_cvt_pk_f32_fp8_e32 v[134:135], v48
	v_cvt_pk_f32_fp8_sdwa v[198:199], v48 src0_sel:WORD_1
	v_cvt_pk_f32_fp8_e32 v[200:201], v49
	v_cvt_pk_f32_fp8_sdwa v[202:203], v49 src0_sel:WORD_1
	s_waitcnt lgkmcnt(0)
	v_pk_fma_f32 v[134:135], v[128:129], v[134:135], v[156:157] op_sel_hi:[0,1,1]
	v_pk_fma_f32 v[156:157], v[128:129], v[198:199], v[186:187] op_sel_hi:[0,1,1]
	v_pk_fma_f32 v[186:187], v[128:129], v[200:201], v[188:189] op_sel_hi:[0,1,1]
	v_pk_fma_f32 v[188:189], v[128:129], v[202:203], v[190:191] op_sel_hi:[0,1,1]
	v_cvt_pk_f32_fp8_e32 v[190:191], v50
	v_cvt_pk_f32_fp8_sdwa v[198:199], v50 src0_sel:WORD_1
	v_cvt_pk_f32_fp8_e32 v[200:201], v51
	v_cvt_pk_f32_fp8_sdwa v[202:203], v51 src0_sel:WORD_1
	v_pk_fma_f32 v[190:191], v[128:129], v[190:191], v[192:193] op_sel_hi:[0,1,1]
	v_pk_fma_f32 v[192:193], v[128:129], v[198:199], v[194:195] op_sel_hi:[0,1,1]
	v_pk_fma_f32 v[194:195], v[128:129], v[200:201], v[196:197] op_sel_hi:[0,1,1]
	v_pk_fma_f32 v[132:133], v[128:129], v[202:203], v[132:133] op_sel_hi:[0,1,1]
	s_waitcnt vmcnt(18)
	v_cvt_pk_f32_fp8_e32 v[196:197], v52
	v_cvt_pk_f32_fp8_sdwa v[198:199], v52 src0_sel:WORD_1
	v_cvt_pk_f32_fp8_e32 v[200:201], v53
	v_cvt_pk_f32_fp8_sdwa v[202:203], v53 src0_sel:WORD_1
	v_pk_fma_f32 v[134:135], v[128:129], v[196:197], v[134:135] op_sel:[1,0,0]
	v_pk_fma_f32 v[156:157], v[128:129], v[198:199], v[156:157] op_sel:[1,0,0]
	v_pk_fma_f32 v[186:187], v[128:129], v[200:201], v[186:187] op_sel:[1,0,0]
	v_pk_fma_f32 v[188:189], v[128:129], v[202:203], v[188:189] op_sel:[1,0,0]
	v_cvt_pk_f32_fp8_e32 v[196:197], v54
	v_cvt_pk_f32_fp8_sdwa v[198:199], v54 src0_sel:WORD_1
	v_cvt_pk_f32_fp8_e32 v[200:201], v55
	v_cvt_pk_f32_fp8_sdwa v[202:203], v55 src0_sel:WORD_1
	v_pk_fma_f32 v[190:191], v[128:129], v[196:197], v[190:191] op_sel:[1,0,0]
	v_pk_fma_f32 v[192:193], v[128:129], v[198:199], v[192:193] op_sel:[1,0,0]
	v_pk_fma_f32 v[194:195], v[128:129], v[200:201], v[194:195] op_sel:[1,0,0]
	v_pk_fma_f32 v[128:129], v[128:129], v[202:203], v[132:133] op_sel:[1,0,0]
	s_waitcnt vmcnt(17)
	v_cvt_pk_f32_fp8_e32 v[132:133], v56
	v_cvt_pk_f32_fp8_sdwa v[196:197], v56 src0_sel:WORD_1
	v_cvt_pk_f32_fp8_e32 v[198:199], v57
	v_cvt_pk_f32_fp8_sdwa v[200:201], v57 src0_sel:WORD_1
	v_pk_fma_f32 v[132:133], v[130:131], v[132:133], v[134:135] op_sel_hi:[0,1,1]
	v_pk_fma_f32 v[134:135], v[130:131], v[196:197], v[156:157] op_sel_hi:[0,1,1]
	v_pk_fma_f32 v[156:157], v[130:131], v[198:199], v[186:187] op_sel_hi:[0,1,1]
	v_pk_fma_f32 v[186:187], v[130:131], v[200:201], v[188:189] op_sel_hi:[0,1,1]
	v_cvt_pk_f32_fp8_e32 v[188:189], v58
	v_cvt_pk_f32_fp8_sdwa v[196:197], v58 src0_sel:WORD_1
	v_cvt_pk_f32_fp8_e32 v[198:199], v59
	v_cvt_pk_f32_fp8_sdwa v[200:201], v59 src0_sel:WORD_1
	v_pk_fma_f32 v[188:189], v[130:131], v[188:189], v[190:191] op_sel_hi:[0,1,1]
	v_pk_fma_f32 v[190:191], v[130:131], v[196:197], v[192:193] op_sel_hi:[0,1,1]
	v_pk_fma_f32 v[192:193], v[130:131], v[198:199], v[194:195] op_sel_hi:[0,1,1]
	s_waitcnt vmcnt(16)
	v_cvt_pk_f32_fp8_e32 v[194:195], v60
	v_pk_fma_f32 v[128:129], v[130:131], v[200:201], v[128:129] op_sel_hi:[0,1,1]
	v_cvt_pk_f32_fp8_sdwa v[196:197], v60 src0_sel:WORD_1
	v_cvt_pk_f32_fp8_e32 v[198:199], v61
	v_cvt_pk_f32_fp8_sdwa v[200:201], v61 src0_sel:WORD_1
	v_mov_b32_e32 v130, v131
	v_pk_fma_f32 v[132:133], v[130:131], v[194:195], v[132:133] op_sel_hi:[0,1,1]
	v_cvt_pk_f32_fp8_e32 v[194:195], v62
	v_pk_fma_f32 v[134:135], v[130:131], v[196:197], v[134:135] op_sel_hi:[0,1,1]
	v_pk_fma_f32 v[156:157], v[130:131], v[198:199], v[156:157] op_sel_hi:[0,1,1]
	v_pk_fma_f32 v[186:187], v[130:131], v[200:201], v[186:187] op_sel_hi:[0,1,1]
	v_cvt_pk_f32_fp8_sdwa v[196:197], v62 src0_sel:WORD_1
	v_cvt_pk_f32_fp8_e32 v[198:199], v63
	v_cvt_pk_f32_fp8_sdwa v[200:201], v63 src0_sel:WORD_1
	v_pk_fma_f32 v[188:189], v[130:131], v[194:195], v[188:189] op_sel_hi:[0,1,1]
	v_pk_fma_f32 v[190:191], v[130:131], v[196:197], v[190:191] op_sel_hi:[0,1,1]
	v_pk_fma_f32 v[192:193], v[130:131], v[198:199], v[192:193] op_sel_hi:[0,1,1]
	v_pk_fma_f32 v[128:129], v[130:131], v[200:201], v[128:129] op_sel_hi:[0,1,1]
	v_cndmask_b32_e64 v131, v132, v188, s[8:9]
	v_cndmask_b32_e64 v130, v188, v132, s[8:9]
	ds_bpermute_b32 v131, v137, v131
	v_cndmask_b32_e64 v132, v133, v189, s[8:9]
	ds_bpermute_b32 v132, v137, v132
	v_cndmask_b32_e64 v140, v134, v190, s[8:9]
	ds_bpermute_b32 v140, v137, v140
	s_waitcnt lgkmcnt(2)
	v_add_f32_e32 v130, v130, v131
	v_cndmask_b32_e64 v131, v189, v133, s[8:9]
	s_waitcnt lgkmcnt(1)
	v_add_f32_e32 v131, v131, v132
	v_cndmask_b32_e64 v132, v190, v134, s[8:9]
	v_cndmask_b32_e64 v134, v135, v191, s[8:9]
	v_cndmask_b32_e64 v133, v191, v135, s[8:9]
	ds_bpermute_b32 v134, v137, v134
	v_cndmask_b32_e64 v135, v156, v192, s[8:9]
	s_waitcnt lgkmcnt(1)
	v_add_f32_e32 v132, v132, v140
	ds_bpermute_b32 v135, v137, v135
	v_cndmask_b32_e64 v140, v157, v193, s[8:9]
	ds_bpermute_b32 v140, v137, v140
	s_waitcnt lgkmcnt(2)
	v_add_f32_e32 v133, v133, v134
	v_cndmask_b32_e64 v134, v192, v156, s[8:9]
	s_waitcnt lgkmcnt(1)
	v_add_f32_e32 v134, v134, v135
	v_cndmask_b32_e64 v135, v193, v157, s[8:9]
	s_waitcnt lgkmcnt(0)
	v_add_f32_e32 v135, v135, v140
	v_cndmask_b32_e64 v140, v128, v186, s[8:9]
	v_cndmask_b32_e64 v128, v186, v128, s[8:9]
	v_cndmask_b32_e64 v155, v187, v129, s[8:9]
	ds_bpermute_b32 v128, v137, v128
	ds_bpermute_b32 v155, v137, v155
	v_cndmask_b32_e64 v129, v129, v187, s[8:9]
	v_cndmask_b32_e64 v156, v130, v134, s[10:11]
	v_cndmask_b32_e64 v130, v134, v130, s[10:11]
	s_waitcnt lgkmcnt(1)
	v_add_f32_e32 v128, v140, v128
	s_waitcnt lgkmcnt(0)
	v_add_f32_e32 v129, v129, v155
	v_cndmask_b32_e64 v134, v135, v131, s[10:11]
	v_cndmask_b32_e64 v131, v131, v135, s[10:11]
	v_cndmask_b32_e64 v135, v132, v128, s[10:11]
	v_cndmask_b32_e64 v140, v133, v129, s[10:11]
	ds_bpermute_b32 v156, v138, v156
	ds_bpermute_b32 v131, v138, v131
	ds_bpermute_b32 v135, v138, v135
	ds_bpermute_b32 v140, v138, v140
	v_cndmask_b32_e64 v128, v128, v132, s[10:11]
	v_cndmask_b32_e64 v129, v129, v133, s[10:11]
	s_waitcnt lgkmcnt(3)
	v_add_f32_e32 v130, v130, v156
	s_waitcnt lgkmcnt(2)
	v_add_f32_e32 v131, v134, v131
	s_waitcnt lgkmcnt(1)
	v_add_f32_e32 v128, v128, v135
	s_waitcnt lgkmcnt(0)
	v_add_f32_e32 v129, v129, v140
	v_cndmask_b32_e64 v132, v130, v128, s[12:13]
	v_cndmask_b32_e64 v133, v131, v129, s[12:13]
	s_or_b32 s30, s30, s2
	ds_bpermute_b32 v132, v136, v132
	ds_bpermute_b32 v133, v136, v133
	s_ashr_i32 s31, s30, 31
	s_and_b32 s57, s53, 0xf80
	s_lshl_b64 s[30:31], s[30:31], 13
	s_add_u32 s30, s64, s30
	s_addc_u32 s31, s65, s31
	s_lshl_b32 s57, s57, 1
	v_cndmask_b32_e64 v128, v128, v130, s[12:13]
	v_cndmask_b32_e64 v129, v129, v131, s[12:13]
	s_add_u32 s30, s30, s57
	s_waitcnt lgkmcnt(1)
	v_add_f32_e32 v128, v128, v132
	s_waitcnt lgkmcnt(0)
	v_add_f32_e32 v129, v129, v133
	s_addc_u32 s31, s31, 0
	v_lshlrev_b32_e32 v140, 1, v142
	v_cvt_pk_bf16_f32 v130, v128, v129
	v_lshl_add_u64 v[128:129], s[30:31], 0, v[140:141]
	v_mov_b32_e32 v155, v141
	v_lshl_add_u64 v[128:129], v[128:129], 0, v[154:155]
	global_store_dword v[128:129], v130, off nt
	s_cmpk_gt_u32 s54, 0xfd
	s_cselect_b64 s[30:31], -1, 0
	s_and_b64 vcc, exec, s[30:31]
	v_and_or_b32 v0, s3, 48, v158
	v_lshl_add_u32 v0, v0, 5, s34
	ds_read_b128 v[22:25], v0
	ds_read_b128 v[54:57], v0 offset:16
	s_and_b32 s57, s22, 0x7e00000
	s_add_u32 s58, s14, s57
	s_addc_u32 s59, s15, 0
	s_waitcnt lgkmcnt(1)
	v_lshlrev_b32_e32 v0, 7, v22
	v_bfe_u32 v1, v22, 16, 16
	v_lshlrev_b32_e32 v8, 7, v23
	v_bfe_u32 v9, v23, 16, 16
	v_lshlrev_b32_e32 v16, 7, v24
	v_bfe_u32 v17, v24, 16, 16
	v_lshlrev_b32_e32 v24, 7, v25
	v_bfe_u32 v25, v25, 16, 16
	s_waitcnt lgkmcnt(0)
	v_lshlrev_b32_e32 v32, 7, v54
	v_bfe_u32 v33, v54, 16, 16
	v_lshlrev_b32_e32 v40, 7, v55
	v_bfe_u32 v41, v55, 16, 16
	v_lshlrev_b32_e32 v48, 7, v56
	v_bfe_u32 v49, v56, 16, 16
	v_lshlrev_b32_e32 v56, 7, v57
	v_bfe_u32 v57, v57, 16, 16
	v_and_or_b32 v0, v0, s36, v142
	v_lshl_or_b32 v4, v1, 7, v142
	v_and_or_b32 v8, v8, s36, v142
	v_lshl_or_b32 v12, v9, 7, v142
	v_and_or_b32 v16, v16, s36, v142
	v_lshl_or_b32 v20, v17, 7, v142
	v_and_or_b32 v24, v24, s36, v142
	v_lshl_or_b32 v28, v25, 7, v142
	v_and_or_b32 v32, v32, s36, v142
	v_lshl_or_b32 v36, v33, 7, v142
	v_and_or_b32 v40, v40, s36, v142
	v_lshl_or_b32 v44, v41, 7, v142
	v_and_or_b32 v48, v48, s36, v142
	v_lshl_or_b32 v52, v49, 7, v142
	v_and_or_b32 v56, v56, s36, v142
	v_lshl_or_b32 v60, v57, 7, v142
	global_load_dwordx4 v[0:3], v0, s[58:59]
	s_nop 0
	global_load_dwordx4 v[4:7], v4, s[58:59]
	s_nop 0
	global_load_dwordx4 v[8:11], v8, s[58:59]
	s_nop 0
	global_load_dwordx4 v[12:15], v12, s[58:59]
	s_nop 0
	global_load_dwordx4 v[16:19], v16, s[58:59]
	s_nop 0
	global_load_dwordx4 v[20:23], v20, s[58:59]
	s_nop 0
	global_load_dwordx4 v[24:27], v24, s[58:59]
	s_nop 0
	global_load_dwordx4 v[28:31], v28, s[58:59]
	s_nop 0
	global_load_dwordx4 v[32:35], v32, s[58:59]
	s_nop 0
	global_load_dwordx4 v[36:39], v36, s[58:59]
	s_nop 0
	global_load_dwordx4 v[40:43], v40, s[58:59]
	s_nop 0
	global_load_dwordx4 v[44:47], v44, s[58:59]
	s_nop 0
	global_load_dwordx4 v[48:51], v48, s[58:59]
	s_nop 0
	global_load_dwordx4 v[52:55], v52, s[58:59]
	s_nop 0
	global_load_dwordx4 v[56:59], v56, s[58:59]
	s_nop 0
	global_load_dwordx4 v[60:63], v60, s[58:59]
	s_branch .LBB0_838
